# v50 + P7: 26 of the 32 loop-invariant LN1/LN2 weight and bias fragment loads hoisted out of the token loop (LN2 tail had 4 dependent load groups per token)
# speedup vs baseline: 1.0098x; 1.0004x over previous
; DI float bflo(unsigned w) { return __uint_as_float(w << 16); }
; DI float bfhi(unsigned w) { return __uint_as_float(w & 0xffff0000u); }
; DI int lane_id() { int l; asm volatile("v_mbcnt_lo_u32_b32 %0, -1, 0\n\tv_mbcnt_hi_u32_b32 %0, -1, %0" : "=v"(l)); return l; }
; DI void p7_ln2(const Ctx& c) {
;     ...
;     const int lane = lane_id();
;     const u16* y1 = (const u16*)(c.ws + WS_Y1); const float* st1 = (const float*)(c.ws + WS_ST1); const u16* yb = (const u16*)(c.ws + WS_YBUF);
;     const float* l1w = kp->in[12]; const float* l1b = kp->in[13]; const float* l2w = kp->in[22]; const float* l2b = kp->in[23];
;     u16* x2b = (u16*)(c.ws + WS_X2B); const float* ssq = (const float*)(c.ws + WS_SSQ); float* rse = (float*)(c.ws + WS_RSE);
;     for (int tb = c.bid; tb < T / 32; tb += c.G)
;     for (int tt = 0; tt < 4; ++tt) { const int tok = tb * 32 + c.wid * 4 + tt;
;         const float mean1 = st1[2 * tok], rstd1 = st1[2 * tok + 1];
;         f32x4 z[8]; float s = 0.f;
; #pragma unroll
;         for (int i = 0; i < 4; ++i) { const int d = (i * 64 + lane) * 8; const u32x4 yr = *(const u32x4*)(y1 + (size_t)tok * D + d);
;             const f32x4 y0 = {bflo(yr.x), bfhi(yr.x), bflo(yr.y), bfhi(yr.y)}, y1v = {bflo(yr.z), bfhi(yr.z), bflo(yr.w), bfhi(yr.w)};
;             const f32x4 g0 = *(const f32x4*)(l1w + d), g1 = *(const f32x4*)(l1w + d + 4), b0 = *(const f32x4*)(l1b + d), b1 = *(const f32x4*)(l1b + d + 4);
;     ...
;             const f32x4 g0 = *(const f32x4*)(l2w + d), g1 = *(const f32x4*)(l2w + d + 4), b0 = *(const f32x4*)(l2b + d), b1 = *(const f32x4*)(l2b + d + 4);
.LBB0_972:
	s_or_b64 exec, exec, s[10:11]
	v_readlane_b32 s4, v242, 4
	v_readlane_b32 s5, v242, 5
	s_mov_b64 s[10:11], s[0:1]
	s_and_b64 vcc, exec, s[4:5]
	s_waitcnt lgkmcnt(0)
	s_barrier
	s_waitcnt vmcnt(22)
	v_mbcnt_lo_u32_b32 v0, -1, 0
	v_mbcnt_hi_u32_b32 v0, -1, v0
	s_cbranch_vccnz .LBB0_981
	s_waitcnt vmcnt(16)
	v_mbcnt_hi_u32_b32 v16, -1, v196
	v_and_b32_e32 v1, 64, v16
	v_add_u32_e32 v17, 64, v1
	v_xor_b32_e32 v18, 32, v16
	s_load_dwordx4 s[12:15], s[10:11], 0xb0
	s_load_dwordx4 s[16:19], s[10:11], 0x60
	v_cmp_lt_i32_e64 s[10:11], v18, v17
	v_lshlrev_b32_e32 v2, 3, v0
	s_waitcnt vmcnt(4)
	v_add_u32_e32 v8, 0x400, v2
	v_cndmask_b32_e64 v18, v16, v18, s[10:11]
	v_lshlrev_b32_e32 v94, 2, v18
	v_xor_b32_e32 v18, 16, v16
	v_cmp_lt_i32_e64 s[10:11], v18, v17
	v_add_u32_e32 v12, 0x600, v2
	v_ashrrev_i32_e32 v3, 31, v2
	v_cndmask_b32_e64 v18, v16, v18, s[10:11]
	v_lshlrev_b32_e32 v95, 2, v18
	v_xor_b32_e32 v18, 8, v16
	v_cmp_lt_i32_e64 s[10:11], v18, v17
	v_ashrrev_i32_e32 v9, 31, v8
	v_ashrrev_i32_e32 v13, 31, v12
	v_cndmask_b32_e64 v18, v16, v18, s[10:11]
	v_lshlrev_b32_e32 v96, 2, v18
	v_xor_b32_e32 v18, 4, v16
	v_cmp_lt_i32_e64 s[10:11], v18, v17
	v_lshlrev_b64 v[4:5], 2, v[2:3]
	v_add_u32_e32 v6, 0x200, v2
	v_cndmask_b32_e64 v18, v16, v18, s[10:11]
	v_lshlrev_b32_e32 v97, 2, v18
	v_xor_b32_e32 v18, 2, v16
	v_cmp_lt_i32_e64 s[10:11], v18, v17
	v_lshlrev_b64 v[10:11], 2, v[8:9]
	v_lshlrev_b64 v[14:15], 2, v[12:13]
	v_cndmask_b32_e64 v18, v16, v18, s[10:11]
	v_lshlrev_b32_e32 v98, 2, v18
	v_xor_b32_e32 v18, 1, v16
	v_cmp_lt_i32_e64 s[10:11], v18, v17
	s_lshl_b32 s4, s89, 2
	s_lshl_b32 s5, s90, 5
	v_ashrrev_i32_e32 v1, 31, v0
	s_waitcnt lgkmcnt(0)
	v_lshl_add_u64 v[24:25], s[16:17], 0, v[4:5]
	v_lshl_add_u64 v[26:27], s[18:19], 0, v[4:5]
	v_ashrrev_i32_e32 v7, 31, v6
	v_cndmask_b32_e64 v16, v16, v18, s[10:11]
	v_lshl_add_u64 v[36:37], s[12:13], 0, v[4:5]
	v_lshl_add_u64 v[38:39], s[14:15], 0, v[4:5]
	v_lshl_add_u64 v[40:41], s[12:13], 0, v[10:11]
	s_waitcnt vmcnt(1)
	v_lshl_add_u64 v[44:45], s[12:13], 0, v[14:15]
	s_add_i32 s12, s5, s4
	v_mov_b64_e32 v[4:5], 0xa510000
	s_lshl_b32 s5, s90, 6
	s_lshl_b32 s10, s89, 3
	v_cmp_gt_i32_e32 vcc, 32, v0
	v_cmp_eq_u32_e64 s[6:7], 0, v0
	v_lshl_add_u64 v[28:29], s[16:17], 0, v[10:11]
	v_lshl_add_u64 v[30:31], s[18:19], 0, v[10:11]
	v_lshl_add_u64 v[32:33], s[16:17], 0, v[14:15]
	v_lshl_add_u64 v[34:35], s[18:19], 0, v[14:15]
	v_lshlrev_b32_e32 v99, 2, v16
	v_lshl_add_u64 v[42:43], s[14:15], 0, v[10:11]
	v_lshl_add_u64 v[46:47], s[14:15], 0, v[14:15]
	s_lshl_b32 s4, s44, 5
	v_lshl_add_u64 v[48:49], v[0:1], 2, v[4:5]
	v_lshlrev_b64 v[50:51], 1, v[2:3]
	s_waitcnt vmcnt(0)
	v_lshlrev_b64 v[52:53], 1, v[6:7]
	v_lshlrev_b64 v[54:55], 1, v[8:9]
	v_lshlrev_b64 v[56:57], 1, v[12:13]
	s_add_i32 s5, s5, s10
	s_lshl_b32 s15, s44, 6
	v_mov_b32_e32 v58, 0
	s_mov_b32 s24, 0x12690000
	s_mov_b32 s25, 0x22ca1000
	s_mov_b32 s26, 0x22ca3000
	s_mov_b32 s14, 0x3f9837f0
	v_mov_b32_e32 v100, 0x3727c5ac
	s_mov_b32 s27, 0x800000
	s_mov_b32 s28, 0x2aca0000
	s_mov_b64 s[16:17], 0x80
	s_mov_b64 s[18:19], 0x4000
	s_mov_b64 s[20:21], 0x1000
	s_mov_b32 s29, s90
	global_load_dwordx4 v[144:147], v[26:27], off offset:2064
	global_load_dwordx4 v[148:151], v[26:27], off offset:2048
	global_load_dwordx4 v[152:155], v[28:29], off offset:16
	global_load_dwordx4 v[156:159], v[28:29], off
	global_load_dwordx4 v[160:163], v[30:31], off offset:16
	global_load_dwordx4 v[164:167], v[30:31], off
	global_load_dwordx4 v[168:171], v[32:33], off offset:16
	global_load_dwordx4 v[172:175], v[32:33], off
	global_load_dwordx4 v[176:179], v[34:35], off offset:16
	global_load_dwordx4 v[180:183], v[34:35], off
	global_load_dwordx4 v[184:187], v[36:37], off offset:16
	global_load_dwordx4 v[188:191], v[36:37], off
	global_load_dwordx4 v[192:195], v[38:39], off offset:16
	global_load_dwordx4 v[196:199], v[38:39], off
	global_load_dwordx4 v[200:203], v[38:39], off offset:2048
	global_load_dwordx4 v[204:207], v[36:37], off offset:2048
	global_load_dwordx4 v[208:211], v[36:37], off offset:2064
	global_load_dwordx4 v[216:219], v[38:39], off offset:2064
	global_load_dwordx4 v[220:223], v[42:43], off
	global_load_dwordx4 v[224:227], v[40:41], off
	global_load_dwordx4 v[230:233], v[40:41], off offset:16
	global_load_dwordx4 v[234:237], v[42:43], off offset:16
	global_load_dwordx4 v[238:241], v[46:47], off
	global_load_dwordx4 v[244:247], v[44:45], off
	global_load_dwordx4 v[248:251], v[44:45], off offset:16
	global_load_dwordx4 v[252:255], v[46:47], off offset:16
	s_waitcnt vmcnt(0)
	s_branch .LBB0_975

; DI float bflo(unsigned w) { return __uint_as_float(w << 16); }
; DI float bfhi(unsigned w) { return __uint_as_float(w & 0xffff0000u); }
; DI void p7_ln2(const Ctx& c) {
;     ...
;     for (int tt = 0; tt < 4; ++tt) { const int tok = tb * 32 + c.wid * 4 + tt;
;         const float mean1 = st1[2 * tok], rstd1 = st1[2 * tok + 1];
;         f32x4 z[8]; float s = 0.f;
; #pragma unroll
;         for (int i = 0; i < 4; ++i) { const int d = (i * 64 + lane) * 8; const u32x4 yr = *(const u32x4*)(y1 + (size_t)tok * D + d);
;             const f32x4 y0 = {bflo(yr.x), bfhi(yr.x), bflo(yr.y), bfhi(yr.y)}, y1v = {bflo(yr.z), bfhi(yr.z), bflo(yr.w), bfhi(yr.w)};
;             const f32x4 g0 = *(const f32x4*)(l1w + d), g1 = *(const f32x4*)(l1w + d + 4), b0 = *(const f32x4*)(l1b + d), b1 = *(const f32x4*)(l1b + d + 4);
;             f32x4 a0 = ((y0 - mean1) * rstd1 * g0 + b0) * DN_ALPHA, a1 = ((y1v - mean1) * rstd1 * g1 + b1) * DN_ALPHA;
; #pragma unroll
;             for (int k = 0; k < 4; ++k) { const u32x4 v = *(const u32x4*)(yb + ((size_t)tok * 4 + k) * D + d);
;                 a0[0] += bflo(v.x); a0[1] += bfhi(v.x); a0[2] += bflo(v.y); a0[3] += bfhi(v.y); a1[0] += bflo(v.z); a1[1] += bfhi(v.z); a1[2] += bflo(v.w); a1[3] += bfhi(v.w); }
;             z[2 * i] = a0; z[2 * i + 1] = a1; s += ((a0[0] + a0[1]) + (a0[2] + a0[3])) + ((a1[0] + a1[1]) + (a1[2] + a1[3])); }
.LBB0_977:
	v_lshl_add_u64 v[72:73], s[34:35], 0, v[70:71]
	v_add_co_u32_e64 v86, s[10:11], s24, v72
	s_waitcnt lgkmcnt(0)
	v_lshl_add_u64 v[0:1], s[34:35], 0, v[62:63]
	v_addc_co_u32_e64 v87, s[10:11], 0, v73, s[10:11]
	global_load_dwordx4 v[16:19], v[86:87], off
	v_add_co_u32_e64 v2, s[10:11], s25, v0
	s_nop 1
	v_addc_co_u32_e64 v3, s[10:11], 0, v1, s[10:11]
	v_add_co_u32_e64 v0, s[10:11], s26, v0
	global_load_dwordx4 v[78:81], v[2:3], off
	s_nop 0
	v_addc_co_u32_e64 v1, s[10:11], 0, v1, s[10:11]
	s_add_i32 s10, s5, s13
	s_ashr_i32 s11, s10, 31
	global_load_dwordx4 v[88:91], v[0:1], off offset:-4096
	global_load_dwordx4 v[102:105], v[0:1], off
	s_lshl_b64 s[10:11], s[10:11], 2
	s_add_u32 s10, s3, s10
	s_addc_u32 s11, s71, s11
	global_load_dwordx2 v[82:83], v58, s[10:11]
	global_load_dwordx4 v[106:109], v[2:3], off offset:-4096
	global_load_dwordx4 v[74:77], v[26:27], off
	global_load_dwordx4 v[110:113], v[24:25], off
	global_load_dwordx4 v[114:117], v[24:25], off offset:16
	global_load_dwordx4 v[118:121], v[26:27], off offset:16
	global_load_dwordx4 v[12:15], v[24:25], off offset:2064
	global_load_dwordx4 v[122:125], v[24:25], off offset:2048
	v_lshl_add_u64 v[0:1], s[34:35], 0, v[64:65]
	v_add_co_u32_e64 v4, s[10:11], s25, v0
	s_waitcnt vmcnt(11)
	v_lshlrev_b32_e32 v59, 16, v16
	v_addc_co_u32_e64 v5, s[10:11], 0, v1, s[10:11]
	v_add_co_u32_e64 v84, s[10:11], s26, v0
	v_and_b32_e32 v101, 0xffff0000, v16
	s_nop 0
	v_addc_co_u32_e64 v85, s[10:11], 0, v1, s[10:11]
	global_load_dwordx4 v[130:133], v[86:87], off offset:1024
	global_load_dwordx4 v[8:11], v[4:5], off offset:-4096
	global_load_dwordx4 v[0:3], v[4:5], off
	s_nop 0
	global_load_dwordx4 v[4:7], v[84:85], off offset:-4096
	v_lshlrev_b32_e32 v134, 16, v17
	v_and_b32_e32 v135, 0xffff0000, v17
	s_waitcnt vmcnt(11)
	v_sub_f32_e32 v135, v135, v82
	v_sub_f32_e32 v134, v134, v82
	v_sub_f32_e32 v137, v101, v82
	v_sub_f32_e32 v136, v59, v82
	v_pk_mul_f32 v[136:137], v[82:83], v[136:137] op_sel:[1,0]
	v_pk_mul_f32 v[134:135], v[82:83], v[134:135] op_sel:[1,0]
	s_waitcnt vmcnt(10)
	v_lshlrev_b32_e32 v142, 16, v106
	v_and_b32_e32 v143, 0xffff0000, v106
	v_lshlrev_b32_e32 v106, 16, v107
	v_and_b32_e32 v107, 0xffff0000, v107
	s_waitcnt vmcnt(8)
	v_pk_fma_f32 v[76:77], v[112:113], v[134:135], v[76:77]
	v_pk_fma_f32 v[74:75], v[110:111], v[136:137], v[74:75]
	v_lshlrev_b32_e32 v16, 16, v78
	v_and_b32_e32 v17, 0xffff0000, v78
	v_lshlrev_b32_e32 v78, 16, v79
	v_and_b32_e32 v79, 0xffff0000, v79
	v_pk_fma_f32 v[74:75], v[74:75], s[14:15], v[142:143] op_sel_hi:[1,0,1]
	v_pk_fma_f32 v[76:77], v[76:77], s[14:15], v[106:107] op_sel_hi:[1,0,1]
	v_lshlrev_b32_e32 v140, 16, v18
	v_and_b32_e32 v141, 0xffff0000, v18
	v_lshlrev_b32_e32 v138, 16, v19
	v_and_b32_e32 v139, 0xffff0000, v19
	v_lshlrev_b32_e32 v18, 16, v88
	v_and_b32_e32 v19, 0xffff0000, v88
	v_lshlrev_b32_e32 v88, 16, v89
	v_and_b32_e32 v89, 0xffff0000, v89
	v_pk_add_f32 v[16:17], v[74:75], v[16:17]
	v_pk_add_f32 v[74:75], v[76:77], v[78:79]
	v_lshlrev_b32_e32 v92, 16, v102
	v_and_b32_e32 v93, 0xffff0000, v102
	v_lshlrev_b32_e32 v102, 16, v103
	v_pk_add_f32 v[16:17], v[16:17], v[18:19]
	v_pk_add_f32 v[18:19], v[74:75], v[88:89]
	v_and_b32_e32 v103, 0xffff0000, v103
	v_pk_add_f32 v[74:75], v[16:17], v[92:93]
	v_pk_add_f32 v[76:77], v[18:19], v[102:103]
	global_load_dwordx4 v[16:19], v[84:85], off
	v_sub_f32_e32 v141, v141, v82
	v_sub_f32_e32 v140, v140, v82
	v_pk_mul_f32 v[140:141], v[82:83], v[140:141] op_sel:[1,0]
	v_lshlrev_b32_e32 v78, 16, v108
	s_waitcnt vmcnt(7)
	v_pk_fma_f32 v[112:113], v[114:115], v[140:141], v[118:119]
	v_and_b32_e32 v79, 0xffff0000, v108
	v_pk_fma_f32 v[78:79], v[112:113], s[14:15], v[78:79] op_sel_hi:[1,0,1]
	v_lshlrev_b32_e32 v84, 16, v80
	v_and_b32_e32 v85, 0xffff0000, v80
	v_sub_f32_e32 v139, v139, v82
	v_sub_f32_e32 v138, v138, v82
	v_pk_add_f32 v[78:79], v[78:79], v[84:85]
	v_lshlrev_b32_e32 v84, 16, v90
	v_and_b32_e32 v85, 0xffff0000, v90
	v_pk_mul_f32 v[138:139], v[82:83], v[138:139] op_sel:[1,0]
	v_pk_add_f32 v[78:79], v[78:79], v[84:85]
	v_lshlrev_b32_e32 v84, 16, v104
	v_and_b32_e32 v85, 0xffff0000, v104
	v_pk_fma_f32 v[110:111], v[116:117], v[138:139], v[120:121]
	v_pk_add_f32 v[78:79], v[78:79], v[84:85]
	v_lshlrev_b32_e32 v84, 16, v109
	v_and_b32_e32 v85, 0xffff0000, v109
	v_pk_fma_f32 v[84:85], v[110:111], s[14:15], v[84:85] op_sel_hi:[1,0,1]
	v_lshlrev_b32_e32 v80, 16, v81
	v_and_b32_e32 v81, 0xffff0000, v81
	v_pk_add_f32 v[80:81], v[84:85], v[80:81]
	v_lshlrev_b32_e32 v84, 16, v91
	v_and_b32_e32 v85, 0xffff0000, v91
	v_pk_add_f32 v[80:81], v[80:81], v[84:85]
	v_lshlrev_b32_e32 v84, 16, v105
	v_and_b32_e32 v85, 0xffff0000, v105
	v_pk_add_f32 v[80:81], v[80:81], v[84:85]
	v_mov_b32_e32 v84, v78
	v_mov_b32_e32 v85, v74
	v_mov_b32_e32 v88, v79
	v_mov_b32_e32 v89, v75
	v_pk_add_f32 v[84:85], v[84:85], v[88:89]
	v_mov_b32_e32 v88, v80
	v_mov_b32_e32 v89, v76
	v_mov_b32_e32 v90, v81
	v_mov_b32_e32 v91, v77
	v_pk_add_f32 v[88:89], v[88:89], v[90:91]
	s_waitcnt vmcnt(4)
	v_lshlrev_b32_e32 v59, 16, v130
	v_pk_add_f32 v[84:85], v[84:85], v[88:89]
	v_sub_f32_e32 v90, v59, v82
	v_pk_add_f32 v[88:89], v[84:85], v[84:85] op_sel:[0,1] op_sel_hi:[1,0]
	v_lshlrev_b32_e32 v84, 16, v131
	v_and_b32_e32 v89, 0xffff0000, v130
	v_and_b32_e32 v85, 0xffff0000, v131
	v_sub_f32_e32 v85, v85, v82
	v_sub_f32_e32 v84, v84, v82
	v_sub_f32_e32 v91, v89, v82
	v_lshlrev_b32_e32 v101, 16, v132
	v_and_b32_e32 v102, 0xffff0000, v132
	v_lshlrev_b32_e32 v103, 16, v133
	v_pk_mul_f32 v[90:91], v[82:83], v[90:91] op_sel:[1,0]
	v_pk_mul_f32 v[84:85], v[82:83], v[84:85] op_sel:[1,0]
	v_and_b32_e32 v104, 0xffff0000, v133
	v_pk_fma_f32 v[92:93], v[124:125], v[84:85], v[150:151]
	v_pk_fma_f32 v[84:85], v[122:123], v[90:91], v[148:149]
	v_sub_f32_e32 v90, v103, v82
	v_sub_f32_e32 v103, v102, v82
	v_sub_f32_e32 v102, v101, v82
	v_sub_f32_e32 v91, v104, v82
	v_pk_mul_f32 v[106:107], v[82:83], v[102:103] op_sel:[1,0]
	global_load_dwordx4 v[102:105], v[86:87], off offset:2048
	v_pk_fma_f32 v[122:123], v[12:13], v[106:107], v[144:145]
	v_pk_mul_f32 v[90:91], v[82:83], v[90:91] op_sel:[1,0]
	s_waitcnt vmcnt(4)
; DI float bflo(unsigned w) { return __uint_as_float(w << 16); }
; DI float bfhi(unsigned w) { return __uint_as_float(w & 0xffff0000u); }
; DI void p7_ln2(const Ctx& c) {
;     ...
;         for (int i = 0; i < 4; ++i) { const int d = (i * 64 + lane) * 8; const u32x4 yr = *(const u32x4*)(y1 + (size_t)tok * D + d);
;             const f32x4 y0 = {bflo(yr.x), bfhi(yr.x), bflo(yr.y), bfhi(yr.y)}, y1v = {bflo(yr.z), bfhi(yr.z), bflo(yr.w), bfhi(yr.w)};
;             const f32x4 g0 = *(const f32x4*)(l1w + d), g1 = *(const f32x4*)(l1w + d + 4), b0 = *(const f32x4*)(l1b + d), b1 = *(const f32x4*)(l1b + d + 4);
;             f32x4 a0 = ((y0 - mean1) * rstd1 * g0 + b0) * DN_ALPHA, a1 = ((y1v - mean1) * rstd1 * g1 + b1) * DN_ALPHA;
; #pragma unroll
;             for (int k = 0; k < 4; ++k) { const u32x4 v = *(const u32x4*)(yb + ((size_t)tok * 4 + k) * D + d);
;                 a0[0] += bflo(v.x); a0[1] += bfhi(v.x); a0[2] += bflo(v.y); a0[3] += bfhi(v.y); a1[0] += bflo(v.z); a1[1] += bfhi(v.z); a1[2] += bflo(v.w); a1[3] += bfhi(v.w); }
;             z[2 * i] = a0; z[2 * i + 1] = a1; s += ((a0[0] + a0[1]) + (a0[2] + a0[3])) + ((a1[0] + a1[1]) + (a1[2] + a1[3])); }
	v_lshlrev_b32_e32 v12, 16, v8
	v_and_b32_e32 v13, 0xffff0000, v8
	v_lshlrev_b32_e32 v8, 16, v9
	v_and_b32_e32 v9, 0xffff0000, v9
	v_pk_fma_f32 v[90:91], v[14:15], v[90:91], v[146:147]
	v_pk_fma_f32 v[12:13], v[84:85], s[14:15], v[12:13] op_sel_hi:[1,0,1]
	s_waitcnt vmcnt(3)
	v_lshlrev_b32_e32 v14, 16, v0
	v_and_b32_e32 v15, 0xffff0000, v0
	v_pk_fma_f32 v[8:9], v[92:93], s[14:15], v[8:9] op_sel_hi:[1,0,1]
	v_lshlrev_b32_e32 v0, 16, v1
	v_and_b32_e32 v1, 0xffff0000, v1
	v_pk_add_f32 v[12:13], v[12:13], v[14:15]
	s_waitcnt vmcnt(2)
	v_lshlrev_b32_e32 v14, 16, v4
	v_and_b32_e32 v15, 0xffff0000, v4
	v_pk_add_f32 v[0:1], v[8:9], v[0:1]
	v_lshlrev_b32_e32 v4, 16, v5
	v_and_b32_e32 v5, 0xffff0000, v5
	v_lshl_add_u64 v[124:125], s[34:35], 0, v[66:67]
	v_pk_add_f32 v[0:1], v[0:1], v[4:5]
	s_waitcnt vmcnt(1)
	v_lshlrev_b32_e32 v4, 16, v17
	v_and_b32_e32 v5, 0xffff0000, v17
	v_add_co_u32_e64 v22, s[10:11], s25, v124
	v_pk_add_f32 v[0:1], v[0:1], v[4:5]
	v_lshlrev_b32_e32 v4, 16, v10
	v_and_b32_e32 v5, 0xffff0000, v10
	v_addc_co_u32_e64 v23, s[10:11], 0, v125, s[10:11]
	v_pk_fma_f32 v[4:5], v[122:123], s[14:15], v[4:5] op_sel_hi:[1,0,1]
	v_lshlrev_b32_e32 v8, 16, v2
	v_and_b32_e32 v9, 0xffff0000, v2
	v_pk_add_f32 v[4:5], v[4:5], v[8:9]
	v_add_co_u32_e64 v8, s[10:11], s26, v124
	v_lshlrev_b32_e32 v84, 16, v16
	v_and_b32_e32 v85, 0xffff0000, v16
	v_addc_co_u32_e64 v9, s[10:11], 0, v125, s[10:11]
	v_lshlrev_b32_e32 v16, 16, v6
	v_and_b32_e32 v17, 0xffff0000, v6
	global_load_dwordx4 v[122:125], v[8:9], off offset:-4096
	global_load_dwordx4 v[126:129], v[8:9], off
	v_pk_add_f32 v[4:5], v[4:5], v[16:17]
	v_lshlrev_b32_e32 v8, 16, v18
	v_and_b32_e32 v9, 0xffff0000, v18
	v_pk_add_f32 v[4:5], v[4:5], v[8:9]
	v_lshlrev_b32_e32 v8, 16, v11
	v_and_b32_e32 v9, 0xffff0000, v11
	v_pk_fma_f32 v[8:9], v[90:91], s[14:15], v[8:9] op_sel_hi:[1,0,1]
	v_lshlrev_b32_e32 v2, 16, v3
	v_and_b32_e32 v3, 0xffff0000, v3
	v_pk_add_f32 v[20:21], v[12:13], v[14:15]
	global_load_dwordx4 v[12:15], v[22:23], off offset:-4096
	v_pk_add_f32 v[2:3], v[8:9], v[2:3]
	v_lshlrev_b32_e32 v6, 16, v7
	v_and_b32_e32 v7, 0xffff0000, v7
	v_pk_add_f32 v[84:85], v[20:21], v[84:85]
	v_pk_add_f32 v[2:3], v[2:3], v[6:7]
	v_lshlrev_b32_e32 v6, 16, v19
	v_and_b32_e32 v7, 0xffff0000, v19
	global_load_dwordx4 v[16:19], v[86:87], off offset:3072
	v_pk_add_f32 v[2:3], v[2:3], v[6:7]
	global_load_dwordx4 v[20:23], v[22:23], off
	v_mov_b32_e32 v6, v84
	v_mov_b32_e32 v7, v0
	v_mov_b32_e32 v8, v85
	v_mov_b32_e32 v9, v1
	v_pk_add_f32 v[6:7], v[6:7], v[8:9]
	v_mov_b32_e32 v8, v5
	v_pk_add_f32 v[90:91], v[6:7], v[6:7] op_sel:[0,1] op_sel_hi:[1,0]
	v_mov_b32_e32 v6, v4
	v_mov_b32_e32 v7, v2
	v_mov_b32_e32 v9, v3
	v_pk_add_f32 v[6:7], v[6:7], v[8:9]
	v_lshl_add_u64 v[134:135], s[34:35], 0, v[68:69]
	v_pk_add_f32 v[92:93], v[6:7], v[6:7] op_sel:[0,1] op_sel_hi:[1,0]
	s_waitcnt vmcnt(5)
	v_lshlrev_b32_e32 v8, 16, v102
	v_and_b32_e32 v9, 0xffff0000, v102
	v_lshlrev_b32_e32 v6, 16, v103
	v_and_b32_e32 v7, 0xffff0000, v103
	v_sub_f32_e32 v7, v7, v82
	v_sub_f32_e32 v6, v6, v82
	v_sub_f32_e32 v9, v9, v82
	v_sub_f32_e32 v8, v8, v82
	v_lshlrev_b32_e32 v59, 16, v104
	v_and_b32_e32 v86, 0xffff0000, v104
	v_lshlrev_b32_e32 v87, 16, v105
	v_and_b32_e32 v89, 0xffff0000, v105
	v_pk_mul_f32 v[8:9], v[82:83], v[8:9] op_sel:[1,0]
	v_pk_mul_f32 v[6:7], v[82:83], v[6:7] op_sel:[1,0]
	v_add_co_u32_e64 v130, s[10:11], s25, v134
	s_waitcnt vmcnt(5)
	v_pk_fma_f32 v[10:11], v[158:159], v[6:7], v[166:167]
	v_pk_fma_f32 v[6:7], v[156:157], v[8:9], v[164:165]
	v_sub_f32_e32 v9, v89, v82
	v_sub_f32_e32 v8, v87, v82
	v_sub_f32_e32 v87, v86, v82
	v_sub_f32_e32 v86, v59, v82
	v_pk_mul_f32 v[86:87], v[82:83], v[86:87] op_sel:[1,0]
	v_pk_mul_f32 v[8:9], v[82:83], v[8:9] op_sel:[1,0]
	v_pk_fma_f32 v[86:87], v[152:153], v[86:87], v[160:161]
	v_pk_fma_f32 v[142:143], v[154:155], v[8:9], v[162:163]
	v_addc_co_u32_e64 v131, s[10:11], 0, v135, s[10:11]
	v_add_co_u32_e64 v138, s[10:11], s26, v134
	global_load_dwordx4 v[118:121], v[130:131], off offset:-4096
	s_nop 0
	global_load_dwordx4 v[130:133], v[130:131], off
	v_addc_co_u32_e64 v139, s[10:11], 0, v135, s[10:11]
	global_load_dwordx4 v[134:137], v[138:139], off offset:-4096
	s_waitcnt vmcnt(5)
	v_lshlrev_b32_e32 v8, 16, v12
	global_load_dwordx4 v[138:141], v[138:139], off
	v_and_b32_e32 v9, 0xffff0000, v12
	v_pk_fma_f32 v[6:7], v[6:7], s[14:15], v[8:9] op_sel_hi:[1,0,1]
	s_waitcnt vmcnt(5)
	v_lshlrev_b32_e32 v59, 16, v19
	s_waitcnt vmcnt(4)
	v_lshlrev_b32_e32 v8, 16, v20
	v_and_b32_e32 v9, 0xffff0000, v20
	v_pk_add_f32 v[6:7], v[6:7], v[8:9]
	v_lshlrev_b32_e32 v8, 16, v122
	v_and_b32_e32 v9, 0xffff0000, v122
	v_pk_add_f32 v[6:7], v[6:7], v[8:9]
	v_lshlrev_b32_e32 v8, 16, v126
	v_and_b32_e32 v9, 0xffff0000, v126
	v_pk_add_f32 v[6:7], v[6:7], v[8:9]
	v_lshlrev_b32_e32 v8, 16, v13
	v_and_b32_e32 v9, 0xffff0000, v13
	v_pk_fma_f32 v[8:9], v[10:11], s[14:15], v[8:9] op_sel_hi:[1,0,1]
	v_lshlrev_b32_e32 v10, 16, v21
	v_and_b32_e32 v11, 0xffff0000, v21
	v_pk_add_f32 v[8:9], v[8:9], v[10:11]
	v_lshlrev_b32_e32 v10, 16, v123
	v_and_b32_e32 v11, 0xffff0000, v123
	v_pk_add_f32 v[8:9], v[8:9], v[10:11]
	v_lshlrev_b32_e32 v10, 16, v127
	v_and_b32_e32 v11, 0xffff0000, v127
	v_pk_add_f32 v[8:9], v[8:9], v[10:11]
	v_lshlrev_b32_e32 v10, 16, v14
	v_and_b32_e32 v11, 0xffff0000, v14
	v_pk_fma_f32 v[10:11], v[86:87], s[14:15], v[10:11] op_sel_hi:[1,0,1]
	v_lshlrev_b32_e32 v12, 16, v22
	v_and_b32_e32 v13, 0xffff0000, v22
	v_pk_add_f32 v[10:11], v[10:11], v[12:13]
	v_lshlrev_b32_e32 v12, 16, v124
	v_and_b32_e32 v13, 0xffff0000, v124
	v_pk_add_f32 v[10:11], v[10:11], v[12:13]
	v_lshlrev_b32_e32 v12, 16, v128
	v_and_b32_e32 v13, 0xffff0000, v128
	v_pk_add_f32 v[10:11], v[10:11], v[12:13]
	v_lshlrev_b32_e32 v12, 16, v15
	v_and_b32_e32 v13, 0xffff0000, v15
	v_pk_fma_f32 v[12:13], v[142:143], s[14:15], v[12:13] op_sel_hi:[1,0,1]
	v_lshlrev_b32_e32 v14, 16, v23
	v_and_b32_e32 v15, 0xffff0000, v23
	v_pk_add_f32 v[12:13], v[12:13], v[14:15]
	v_lshlrev_b32_e32 v14, 16, v125
	v_and_b32_e32 v15, 0xffff0000, v125
	v_pk_add_f32 v[12:13], v[12:13], v[14:15]
	v_lshlrev_b32_e32 v14, 16, v129
	v_and_b32_e32 v15, 0xffff0000, v129
	v_pk_add_f32 v[12:13], v[12:13], v[14:15]
	v_lshlrev_b32_e32 v20, 16, v16
	v_and_b32_e32 v16, 0xffff0000, v16
	v_lshlrev_b32_e32 v14, 16, v17
	v_and_b32_e32 v15, 0xffff0000, v17
	v_pk_add_f32 v[86:87], v[8:9], v[8:9] op_sel:[0,1] op_sel_hi:[1,0]
	v_sub_f32_e32 v15, v15, v82
	v_sub_f32_e32 v14, v14, v82
	v_sub_f32_e32 v17, v16, v82
	v_sub_f32_e32 v16, v20, v82
	v_pk_add_f32 v[22:23], v[6:7], v[6:7] op_sel:[0,1] op_sel_hi:[1,0]
	v_and_b32_e32 v87, 0xffff0000, v19
	v_pk_mul_f32 v[16:17], v[82:83], v[16:17] op_sel:[1,0]
	v_pk_mul_f32 v[14:15], v[82:83], v[14:15] op_sel:[1,0]
	v_lshlrev_b32_e32 v23, 16, v18
	v_and_b32_e32 v21, 0xffff0000, v18
	s_waitcnt vmcnt(4)
; DI void p7_ln2(const Ctx& c) {
;     ...
;             z[2 * i] = a0; z[2 * i + 1] = a1; s += ((a0[0] + a0[1]) + (a0[2] + a0[3])) + ((a1[0] + a1[1]) + (a1[2] + a1[3])); }
; #pragma unroll
;         for (int o = 32; o >= 1; o >>= 1) s += __shfl_xor(s, o);
;         const float mean = s * (1.0f / D); float qv = 0.f;
; #pragma unroll
;         for (int i = 0; i < 8; ++i) { const f32x4 dl = z[i] - mean; qv += (dl[0] * dl[0] + dl[1] * dl[1]) + (dl[2] * dl[2] + dl[3] * dl[3]); }
; #pragma unroll
;         for (int o = 32; o >= 1; o >>= 1) qv += __shfl_xor(qv, o);
;         const float rstd = rsqrtf(qv * (1.0f / D) + LN_EPS);
	v_pk_fma_f32 v[18:19], v[174:175], v[14:15], v[182:183]
	v_pk_fma_f32 v[14:15], v[172:173], v[16:17], v[180:181]
	v_sub_f32_e32 v17, v87, v82
	v_sub_f32_e32 v16, v59, v82
	v_sub_f32_e32 v21, v21, v82
	v_sub_f32_e32 v20, v23, v82
	v_pk_mul_f32 v[16:17], v[82:83], v[16:17] op_sel:[1,0]
	v_pk_mul_f32 v[20:21], v[82:83], v[20:21] op_sel:[1,0]
	v_pk_fma_f32 v[82:83], v[170:171], v[16:17], v[178:179]
	s_waitcnt vmcnt(3)
	v_lshlrev_b32_e32 v16, 16, v118
	v_and_b32_e32 v17, 0xffff0000, v118
	v_pk_fma_f32 v[14:15], v[14:15], s[14:15], v[16:17] op_sel_hi:[1,0,1]
	s_waitcnt vmcnt(2)
	v_lshlrev_b32_e32 v16, 16, v130
	v_and_b32_e32 v17, 0xffff0000, v130
	v_pk_add_f32 v[14:15], v[14:15], v[16:17]
	s_waitcnt vmcnt(1)
	v_lshlrev_b32_e32 v16, 16, v134
	v_and_b32_e32 v17, 0xffff0000, v134
	v_pk_add_f32 v[14:15], v[14:15], v[16:17]
	s_waitcnt vmcnt(0)
	v_lshlrev_b32_e32 v16, 16, v138
	v_and_b32_e32 v17, 0xffff0000, v138
	v_pk_add_f32 v[14:15], v[14:15], v[16:17]
	v_lshlrev_b32_e32 v16, 16, v119
	v_and_b32_e32 v17, 0xffff0000, v119
	v_pk_fma_f32 v[16:17], v[18:19], s[14:15], v[16:17] op_sel_hi:[1,0,1]
	v_lshlrev_b32_e32 v18, 16, v131
	v_and_b32_e32 v19, 0xffff0000, v131
	v_pk_add_f32 v[16:17], v[16:17], v[18:19]
	v_lshlrev_b32_e32 v18, 16, v135
	v_and_b32_e32 v19, 0xffff0000, v135
	v_pk_add_f32 v[16:17], v[16:17], v[18:19]
	v_lshlrev_b32_e32 v18, 16, v139
	v_and_b32_e32 v19, 0xffff0000, v139
	v_pk_fma_f32 v[20:21], v[168:169], v[20:21], v[176:177]
	v_pk_add_f32 v[16:17], v[16:17], v[18:19]
	v_lshlrev_b32_e32 v18, 16, v120
	v_and_b32_e32 v19, 0xffff0000, v120
	v_pk_fma_f32 v[18:19], v[20:21], s[14:15], v[18:19] op_sel_hi:[1,0,1]
	v_lshlrev_b32_e32 v20, 16, v132
	v_and_b32_e32 v21, 0xffff0000, v132
	v_pk_add_f32 v[18:19], v[18:19], v[20:21]
	v_lshlrev_b32_e32 v20, 16, v136
	v_and_b32_e32 v21, 0xffff0000, v136
	v_pk_add_f32 v[18:19], v[18:19], v[20:21]
	v_lshlrev_b32_e32 v20, 16, v140
	v_and_b32_e32 v21, 0xffff0000, v140
	v_pk_add_f32 v[18:19], v[18:19], v[20:21]
	v_lshlrev_b32_e32 v20, 16, v121
	v_and_b32_e32 v21, 0xffff0000, v121
	v_pk_fma_f32 v[20:21], v[82:83], s[14:15], v[20:21] op_sel_hi:[1,0,1]
	v_lshlrev_b32_e32 v82, 16, v133
	v_and_b32_e32 v83, 0xffff0000, v133
	v_pk_add_f32 v[20:21], v[20:21], v[82:83]
	v_lshlrev_b32_e32 v82, 16, v137
	v_and_b32_e32 v83, 0xffff0000, v137
	v_pk_add_f32 v[122:123], v[10:11], v[10:11] op_sel:[0,1] op_sel_hi:[1,0]
	v_pk_add_f32 v[124:125], v[12:13], v[12:13] op_sel:[0,1] op_sel_hi:[1,0]
	v_pk_add_f32 v[20:21], v[20:21], v[82:83]
	v_lshlrev_b32_e32 v82, 16, v141
	v_and_b32_e32 v83, 0xffff0000, v141
	v_pk_add_f32 v[20:21], v[20:21], v[82:83]
	v_mov_b32_e32 v123, v14
	v_mov_b32_e32 v125, v15
	v_mov_b32_e32 v23, v16
	v_mov_b32_e32 v87, v17
	v_pk_add_f32 v[82:83], v[122:123], v[124:125]
	v_pk_add_f32 v[22:23], v[22:23], v[86:87]
	v_mov_b32_e32 v89, v18
	v_mov_b32_e32 v59, v19
	v_mov_b32_e32 v93, v20
	v_mov_b32_e32 v91, v21
	v_pk_add_f32 v[22:23], v[82:83], v[22:23]
	v_pk_add_f32 v[82:83], v[88:89], v[58:59]
	v_pk_add_f32 v[86:87], v[92:93], v[90:91]
	s_nop 0
	v_pk_add_f32 v[82:83], v[82:83], v[86:87]
	s_nop 0
	v_pk_add_f32 v[22:23], v[82:83], v[22:23]
	s_nop 0
	v_add_f32_e32 v22, v22, v23
	ds_bpermute_b32 v23, v94, v22
	s_waitcnt lgkmcnt(0)
	v_add_f32_e32 v22, v22, v23
	ds_bpermute_b32 v23, v95, v22
	s_waitcnt lgkmcnt(0)
	v_add_f32_e32 v22, v22, v23
	ds_bpermute_b32 v23, v96, v22
	s_waitcnt lgkmcnt(0)
	v_add_f32_e32 v22, v22, v23
	ds_bpermute_b32 v23, v97, v22
	s_waitcnt lgkmcnt(0)
	v_add_f32_e32 v22, v22, v23
	ds_bpermute_b32 v23, v98, v22
	s_waitcnt lgkmcnt(0)
	v_add_f32_e32 v22, v22, v23
	ds_bpermute_b32 v23, v99, v22
	s_waitcnt lgkmcnt(0)
	v_add_f32_e32 v59, v22, v23
	v_fmamk_f32 v75, v59, 0xba000000, v75
	v_fmamk_f32 v79, v59, 0xba000000, v79
	v_fmamk_f32 v77, v59, 0xba000000, v77
	v_fmac_f32_e32 v74, 0xba000000, v59
	v_fmamk_f32 v81, v59, 0xba000000, v81
	v_fmac_f32_e32 v78, 0xba000000, v59
	v_mov_b32_e32 v82, v75
	v_mov_b32_e32 v83, v79
	v_fmac_f32_e32 v76, 0xba000000, v59
	v_fmac_f32_e32 v80, 0xba000000, v59
	v_mov_b32_e32 v22, v74
	v_mov_b32_e32 v23, v78
	v_pk_mul_f32 v[82:83], v[82:83], v[82:83]
	v_mov_b32_e32 v86, v77
	v_mov_b32_e32 v87, v81
	v_pk_fma_f32 v[22:23], v[22:23], v[22:23], v[82:83]
	v_mov_b32_e32 v82, v76
	v_mov_b32_e32 v83, v80
	v_pk_mul_f32 v[86:87], v[86:87], v[86:87]
	v_fmamk_f32 v85, v59, 0xba000000, v85
	v_pk_fma_f32 v[82:83], v[82:83], v[82:83], v[86:87]
	v_fmac_f32_e32 v84, 0xba000000, v59
	v_pk_add_f32 v[22:23], v[22:23], v[82:83]
	v_fmamk_f32 v1, v59, 0xba000000, v1
	v_fmac_f32_e32 v0, 0xba000000, v59
	v_pk_add_f32 v[22:23], v[22:23], v[22:23] op_sel_hi:[0,1]
	v_pk_mul_f32 v[82:83], v[0:1], v[0:1]
	v_pk_mul_f32 v[86:87], v[84:85], v[84:85]
	v_fmac_f32_e32 v4, 0xba000000, v59
	v_pk_mov_b32 v[88:89], v[86:87], v[82:83] op_sel:[1,0]
	v_mov_b32_e32 v87, v83
	v_fmamk_f32 v5, v59, 0xba000000, v5
	v_fmac_f32_e32 v2, 0xba000000, v59
	v_mul_f32_e32 v22, v4, v4
	v_pk_add_f32 v[82:83], v[88:89], v[86:87]
	v_fmamk_f32 v3, v59, 0xba000000, v3
	v_pk_fma_f32 v[86:87], v[4:5], v[4:5], v[22:23] op_sel_hi:[1,1,0]
	v_mul_f32_e32 v22, v2, v2
	v_pk_add_f32 v[82:83], v[82:83], v[82:83] op_sel_hi:[0,1]
	v_pk_fma_f32 v[88:89], v[2:3], v[2:3], v[22:23] op_sel_hi:[1,1,0]
	v_fmamk_f32 v9, v59, 0xba000000, v9
	v_fmac_f32_e32 v8, 0xba000000, v59
	v_fmamk_f32 v7, v59, 0xba000000, v7
	v_fmac_f32_e32 v6, 0xba000000, v59
	v_mul_f32_e32 v86, v6, v6
	v_mul_f32_e32 v88, v7, v7
	v_mul_f32_e32 v82, v8, v8
	v_mul_f32_e32 v22, v9, v9
	v_pk_add_f32 v[86:87], v[86:87], v[88:89]
	v_pk_add_f32 v[22:23], v[82:83], v[22:23]
	v_fmamk_f32 v11, v59, 0xba000000, v11
	v_pk_add_f32 v[22:23], v[86:87], v[22:23]
	v_fmac_f32_e32 v10, 0xba000000, v59
	v_fmamk_f32 v13, v59, 0xba000000, v13
	v_fmac_f32_e32 v12, 0xba000000, v59
	v_pk_add_f32 v[22:23], v[22:23], v[22:23] op_sel_hi:[0,1]
	v_pk_mul_f32 v[82:83], v[12:13], v[12:13]
	v_pk_mul_f32 v[110:111], v[10:11], v[10:11]
	v_fmac_f32_e32 v14, 0xba000000, v59
	v_pk_mov_b32 v[112:113], v[110:111], v[82:83] op_sel:[1,0]
	v_mov_b32_e32 v111, v83
	v_fmamk_f32 v15, v59, 0xba000000, v15
	v_fmac_f32_e32 v16, 0xba000000, v59
	v_mul_f32_e32 v22, v14, v14
	v_pk_add_f32 v[82:83], v[112:113], v[110:111]
	v_fmamk_f32 v17, v59, 0xba000000, v17
	v_pk_fma_f32 v[110:111], v[14:15], v[14:15], v[22:23] op_sel_hi:[1,1,0]
	v_mul_f32_e32 v22, v16, v16
	v_pk_add_f32 v[82:83], v[82:83], v[82:83] op_sel_hi:[0,1]
	v_pk_fma_f32 v[112:113], v[16:17], v[16:17], v[22:23] op_sel_hi:[1,1,0]
	v_fmamk_f32 v21, v59, 0xba000000, v21
	v_fmac_f32_e32 v20, 0xba000000, v59
	v_fmamk_f32 v19, v59, 0xba000000, v19
	v_fmac_f32_e32 v18, 0xba000000, v59
	v_mul_f32_e32 v110, v18, v18
	v_mul_f32_e32 v112, v19, v19
	v_mul_f32_e32 v82, v20, v20
	v_mul_f32_e32 v22, v21, v21
	v_pk_add_f32 v[110:111], v[110:111], v[112:113]
	v_pk_add_f32 v[22:23], v[82:83], v[22:23]
	s_nop 0
	v_pk_add_f32 v[22:23], v[110:111], v[22:23]
	s_nop 0
	v_add_f32_e32 v22, v22, v23
	ds_bpermute_b32 v23, v94, v22
	s_waitcnt lgkmcnt(0)
; DI u32x2 pack4(f32x4 v) { bf16x4_t r = __builtin_convertvector(v, bf16x4_t); return __builtin_bit_cast(u32x2, r); }
; DI void p7_ln2(const Ctx& c) {
;     ...
;         const float rstd = rsqrtf(qv * (1.0f / D) + LN_EPS);
; #pragma unroll
;         for (int i = 0; i < 4; ++i) { const int d = (i * 64 + lane) * 8;
;             const f32x4 g0 = *(const f32x4*)(l2w + d), g1 = *(const f32x4*)(l2w + d + 4), b0 = *(const f32x4*)(l2b + d), b1 = *(const f32x4*)(l2b + d + 4);
;             const u32x2 lo = pack4((z[2 * i] - mean) * rstd * g0 + b0), hi = pack4((z[2 * i + 1] - mean) * rstd * g1 + b1);
;             *(u32x4*)(x2b + (size_t)tok * D + d) = (u32x4){lo.x, lo.y, hi.x, hi.y}; }
	v_add_f32_e32 v22, v22, v23
	ds_bpermute_b32 v23, v95, v22
	s_waitcnt lgkmcnt(0)
	v_add_f32_e32 v22, v22, v23
	ds_bpermute_b32 v23, v96, v22
	s_waitcnt lgkmcnt(0)
	v_add_f32_e32 v22, v22, v23
	ds_bpermute_b32 v23, v97, v22
	s_waitcnt lgkmcnt(0)
	v_add_f32_e32 v22, v22, v23
	ds_bpermute_b32 v23, v98, v22
	s_waitcnt lgkmcnt(0)
	v_add_f32_e32 v22, v22, v23
	ds_bpermute_b32 v23, v99, v22
	s_waitcnt lgkmcnt(0)
	v_add_f32_e32 v22, v22, v23
	v_fmamk_f32 v22, v22, 0x3a000000, v100
	v_mul_f32_e32 v23, 0x4b800000, v22
	v_cmp_gt_f32_e64 s[10:11], s27, v22
	s_nop 1
	v_cndmask_b32_e64 v22, v22, v23, s[10:11]
	v_rsq_f32_e32 v22, v22
	s_nop 0
	v_mul_f32_e32 v23, 0x45800000, v22
	v_cndmask_b32_e64 v22, v22, v23, s[10:11]
	v_pk_mul_f32 v[76:77], v[76:77], v[22:23] op_sel_hi:[1,0]
	v_pk_mul_f32 v[74:75], v[74:75], v[22:23] op_sel_hi:[1,0]
	v_pk_mul_f32 v[78:79], v[78:79], v[22:23] op_sel_hi:[1,0]
	s_waitcnt vmcnt(0)
	v_pk_fma_f32 v[82:83], v[188:189], v[74:75], v[196:197]
	v_pk_fma_f32 v[74:75], v[190:191], v[76:77], v[198:199]
	v_pk_mul_f32 v[76:77], v[80:81], v[22:23] op_sel_hi:[1,0]
	v_pk_fma_f32 v[78:79], v[184:185], v[78:79], v[192:193]
	v_pk_fma_f32 v[76:77], v[186:187], v[76:77], v[194:195]
	v_add_co_u32_e64 v90, s[10:11], s28, v72
	v_cvt_pk_bf16_f32 v75, v74, v75
	v_cvt_pk_bf16_f32 v74, v82, v83
	v_cvt_pk_bf16_f32 v77, v76, v77
	v_cvt_pk_bf16_f32 v76, v78, v79
	v_addc_co_u32_e64 v91, s[10:11], 0, v73, s[10:11]
	global_store_dwordx4 v[90:91], v[74:77], off
	s_nop 0
	v_pk_mul_f32 v[84:85], v[84:85], v[22:23] op_sel_hi:[1,0]
	v_pk_mul_f32 v[0:1], v[0:1], v[22:23] op_sel_hi:[1,0]
	v_pk_mul_f32 v[4:5], v[4:5], v[22:23] op_sel_hi:[1,0]
	v_pk_mul_f32 v[2:3], v[2:3], v[22:23] op_sel_hi:[1,0]
	s_waitcnt vmcnt(1)
	v_pk_fma_f32 v[74:75], v[206:207], v[0:1], v[202:203]
	v_pk_fma_f32 v[0:1], v[204:205], v[84:85], v[200:201]
	s_waitcnt vmcnt(1)
	v_pk_fma_f32 v[72:73], v[210:211], v[2:3], v[218:219]
	v_pk_fma_f32 v[2:3], v[208:209], v[4:5], v[216:217]
	v_cvt_pk_bf16_f32 v0, v0, v1
	v_cvt_pk_bf16_f32 v1, v74, v75
	v_cvt_pk_bf16_f32 v2, v2, v3
	v_cvt_pk_bf16_f32 v3, v72, v73
	global_store_dwordx4 v[90:91], v[0:3], off offset:1024
	s_nop 0
	v_pk_mul_f32 v[4:5], v[6:7], v[22:23] op_sel_hi:[1,0]
	v_pk_mul_f32 v[6:7], v[8:9], v[22:23] op_sel_hi:[1,0]
	s_waitcnt vmcnt(2)
	v_pk_fma_f32 v[0:1], v[224:225], v[4:5], v[220:221]
	v_pk_fma_f32 v[2:3], v[226:227], v[6:7], v[222:223]
	v_cvt_pk_bf16_f32 v0, v0, v1
	v_cvt_pk_bf16_f32 v1, v2, v3
	v_pk_mul_f32 v[2:3], v[10:11], v[22:23] op_sel_hi:[1,0]
	v_pk_mul_f32 v[4:5], v[12:13], v[22:23] op_sel_hi:[1,0]
	s_waitcnt vmcnt(2)
	v_pk_fma_f32 v[2:3], v[230:231], v[2:3], v[234:235]
	v_pk_fma_f32 v[4:5], v[232:233], v[4:5], v[236:237]
	v_cvt_pk_bf16_f32 v2, v2, v3
	v_cvt_pk_bf16_f32 v3, v4, v5
	global_store_dwordx4 v[90:91], v[0:3], off offset:2048
	s_nop 0
	v_pk_mul_f32 v[12:13], v[14:15], v[22:23] op_sel_hi:[1,0]
	v_pk_mul_f32 v[14:15], v[16:17], v[22:23] op_sel_hi:[1,0]
	s_waitcnt vmcnt(3)
	v_pk_fma_f32 v[0:1], v[244:245], v[12:13], v[238:239]
	v_pk_fma_f32 v[2:3], v[246:247], v[14:15], v[240:241]
	v_cvt_pk_bf16_f32 v0, v0, v1
	v_cvt_pk_bf16_f32 v1, v2, v3
	v_pk_mul_f32 v[2:3], v[18:19], v[22:23] op_sel_hi:[1,0]
	v_pk_mul_f32 v[4:5], v[20:21], v[22:23] op_sel_hi:[1,0]
	s_waitcnt vmcnt(3)
	v_pk_fma_f32 v[2:3], v[248:249], v[2:3], v[252:253]
	v_pk_fma_f32 v[4:5], v[250:251], v[4:5], v[254:255]
	v_cvt_pk_bf16_f32 v2, v2, v3
	v_cvt_pk_bf16_f32 v3, v4, v5
	global_store_dwordx4 v[90:91], v[0:3], off offset:3072
	s_nop 1
	v_mov_b32_e32 v0, 0
	s_and_saveexec_b64 s[10:11], vcc
	s_cbranch_execz .LBB0_979
	v_lshl_add_u64 v[0:1], s[34:35], 0, v[60:61]
	global_load_dword v0, v[0:1], off
